# P4b merge epilogue rewritten by hand: all 128 sigmoids first (in place, packed f32, runs under the Y load latency), then per-group fma/cvt with Y two groups ahead
# speedup vs baseline: 1.0037x; 1.0034x over previous
.LBB0_802:
	s_cmp_gt_u32 s0, 7
	s_cselect_b64 s[34:35], -1, 0
	s_lshl_b32 s1, s0, 8
	s_and_b32 s26, s1, 0xfffffc00
	s_ashr_i32 s27, s26, 31
	s_and_b32 s19, s1, 0x300
	s_lshl_b64 s[30:31], s[26:27], 2
	v_or_b32_e32 v0, s19, v191
	s_add_u32 s30, s56, s30
	v_lshl_add_u32 v162, s28, 8, v190
	v_mov_b64_e32 v[18:19], s[12:13]
	s_movk_i32 s66, 0x1800
	s_addc_u32 s31, s57, s31
	v_lshlrev_b32_e32 v6, 2, v0
	v_mad_i64_i32 v[18:19], s[28:29], v162, s66, v[18:19]
	s_nop 15
	s_nop 3
	global_load_dwordx4 v[10:13], v6, s[30:31] offset:16
	global_load_dwordx4 v[14:17], v6, s[30:31]
	global_load_dwordx4 v[2:5], v6, s[30:31] offset:528
	s_nop 0
	global_load_dwordx4 v[6:9], v6, s[30:31] offset:512
	v_lshl_add_u64 v[18:19], s[26:27], 1, v[18:19]
	v_lshlrev_b32_e32 v0, 1, v0
	v_lshl_add_u64 v[18:19], v[18:19], 0, v[0:1]
	s_mov_b32 s37, 0
	global_load_dwordx4 v[24:27], v[18:19], off
	global_load_dwordx4 v[28:31], v[18:19], off offset:256
	s_mov_b32 s36, 0x18000
	v_lshl_add_u64 v[22:23], v[18:19], 0, s[36:37]
	global_load_dwordx4 v[164:167], v[22:23], off
	global_load_dwordx4 v[168:171], v[22:23], off offset:256
	v_ashrrev_i32_e32 v163, 31, v162
	s_cmp_gt_u32 s0, 3
	s_cselect_b64 s[28:29], -1, 0
	v_lshlrev_b64 v[20:21], 11, v[162:163]
	v_readlane_b32 s68, v253, 41
	v_lshl_add_u64 v[178:179], s[10:11], 0, v[20:21]
	v_readlane_b32 s69, v253, 42
	v_readlane_b32 s67, v253, 52
	s_not_b64 s[0:1], s[28:29]
	s_mov_b32 s70, 0xe000
	v_lshl_add_u64 v[20:21], v[178:179], 0, v[0:1]
	v_lshl_add_u32 v222, s86, 6, v213
	v_lshlrev_b32_e32 v222, 4, v222
	v_add_u32_e32 v222, 0x200c0, v222
	s_mov_b32 s30, 0xbfb8aa3b
	s_waitcnt vmcnt(4)
	v_pk_add_f32 v[158:159], v[158:159], v[14:15]
	v_pk_add_f32 v[160:161], v[160:161], v[16:17]
	v_pk_add_f32 v[154:155], v[154:155], v[10:11]
	v_pk_add_f32 v[156:157], v[156:157], v[12:13]
	v_pk_mul_f32 v[172:173], v[158:159], s[30:31] op_sel_hi:[1,0]
	v_pk_mul_f32 v[174:175], v[160:161], s[30:31] op_sel_hi:[1,0]
	v_pk_mul_f32 v[176:177], v[154:155], s[30:31] op_sel_hi:[1,0]
	v_pk_mul_f32 v[180:181], v[156:157], s[30:31] op_sel_hi:[1,0]
	v_exp_f32_e32 v172, v172
	v_exp_f32_e32 v173, v173
	v_exp_f32_e32 v174, v174
	v_exp_f32_e32 v175, v175
	v_exp_f32_e32 v176, v176
	v_exp_f32_e32 v177, v177
	v_exp_f32_e32 v180, v180
	v_exp_f32_e32 v181, v181
	v_pk_add_f32 v[172:173], v[172:173], 1.0 op_sel_hi:[1,0]
	v_pk_add_f32 v[174:175], v[174:175], 1.0 op_sel_hi:[1,0]
	v_pk_add_f32 v[176:177], v[176:177], 1.0 op_sel_hi:[1,0]
	v_pk_add_f32 v[180:181], v[180:181], 1.0 op_sel_hi:[1,0]
	v_rcp_f32_e32 v158, v172
	v_rcp_f32_e32 v159, v173
	v_rcp_f32_e32 v160, v174
	v_rcp_f32_e32 v161, v175
	v_rcp_f32_e32 v154, v176
	v_rcp_f32_e32 v155, v177
	v_rcp_f32_e32 v156, v180
	v_rcp_f32_e32 v157, v181
	v_pk_add_f32 v[150:151], v[150:151], v[6:7]
	v_pk_add_f32 v[152:153], v[152:153], v[8:9]
	v_pk_add_f32 v[146:147], v[146:147], v[2:3]
	v_pk_add_f32 v[148:149], v[148:149], v[4:5]
	v_pk_mul_f32 v[172:173], v[150:151], s[30:31] op_sel_hi:[1,0]
	v_pk_mul_f32 v[174:175], v[152:153], s[30:31] op_sel_hi:[1,0]
	v_pk_mul_f32 v[176:177], v[146:147], s[30:31] op_sel_hi:[1,0]
	v_pk_mul_f32 v[180:181], v[148:149], s[30:31] op_sel_hi:[1,0]
	v_exp_f32_e32 v172, v172
	v_exp_f32_e32 v173, v173
	v_exp_f32_e32 v174, v174
	v_exp_f32_e32 v175, v175
	v_exp_f32_e32 v176, v176
	v_exp_f32_e32 v177, v177
	v_exp_f32_e32 v180, v180
	v_exp_f32_e32 v181, v181
	v_pk_add_f32 v[172:173], v[172:173], 1.0 op_sel_hi:[1,0]
	v_pk_add_f32 v[174:175], v[174:175], 1.0 op_sel_hi:[1,0]
	v_pk_add_f32 v[176:177], v[176:177], 1.0 op_sel_hi:[1,0]
	v_pk_add_f32 v[180:181], v[180:181], 1.0 op_sel_hi:[1,0]
	v_rcp_f32_e32 v150, v172
	v_rcp_f32_e32 v151, v173
	v_rcp_f32_e32 v152, v174
	v_rcp_f32_e32 v153, v175
	v_rcp_f32_e32 v146, v176
	v_rcp_f32_e32 v147, v177
	v_rcp_f32_e32 v148, v180
	v_rcp_f32_e32 v149, v181
	v_pk_add_f32 v[142:143], v[142:143], v[14:15]
	v_pk_add_f32 v[144:145], v[144:145], v[16:17]
	v_pk_add_f32 v[138:139], v[138:139], v[10:11]
	v_pk_add_f32 v[140:141], v[140:141], v[12:13]
	v_pk_mul_f32 v[172:173], v[142:143], s[30:31] op_sel_hi:[1,0]
	v_pk_mul_f32 v[174:175], v[144:145], s[30:31] op_sel_hi:[1,0]
	v_pk_mul_f32 v[176:177], v[138:139], s[30:31] op_sel_hi:[1,0]
	v_pk_mul_f32 v[180:181], v[140:141], s[30:31] op_sel_hi:[1,0]
	v_exp_f32_e32 v172, v172
	v_exp_f32_e32 v173, v173
	v_exp_f32_e32 v174, v174
	v_exp_f32_e32 v175, v175
	v_exp_f32_e32 v176, v176
	v_exp_f32_e32 v177, v177
	v_exp_f32_e32 v180, v180
	v_exp_f32_e32 v181, v181
	v_pk_add_f32 v[172:173], v[172:173], 1.0 op_sel_hi:[1,0]
	v_pk_add_f32 v[174:175], v[174:175], 1.0 op_sel_hi:[1,0]
	v_pk_add_f32 v[176:177], v[176:177], 1.0 op_sel_hi:[1,0]
	v_pk_add_f32 v[180:181], v[180:181], 1.0 op_sel_hi:[1,0]
	v_rcp_f32_e32 v142, v172
	v_rcp_f32_e32 v143, v173
	v_rcp_f32_e32 v144, v174
	v_rcp_f32_e32 v145, v175
	v_rcp_f32_e32 v138, v176
	v_rcp_f32_e32 v139, v177
	v_rcp_f32_e32 v140, v180
	v_rcp_f32_e32 v141, v181
	v_pk_add_f32 v[134:135], v[134:135], v[6:7]
	v_pk_add_f32 v[136:137], v[136:137], v[8:9]
	v_pk_add_f32 v[130:131], v[130:131], v[2:3]
	v_pk_add_f32 v[132:133], v[132:133], v[4:5]
	v_pk_mul_f32 v[172:173], v[134:135], s[30:31] op_sel_hi:[1,0]
	v_pk_mul_f32 v[174:175], v[136:137], s[30:31] op_sel_hi:[1,0]
	v_pk_mul_f32 v[176:177], v[130:131], s[30:31] op_sel_hi:[1,0]
	v_pk_mul_f32 v[180:181], v[132:133], s[30:31] op_sel_hi:[1,0]
	v_exp_f32_e32 v172, v172
	v_exp_f32_e32 v173, v173
	v_exp_f32_e32 v174, v174
	v_exp_f32_e32 v175, v175
	v_exp_f32_e32 v176, v176
	v_exp_f32_e32 v177, v177
	v_exp_f32_e32 v180, v180
	v_exp_f32_e32 v181, v181
	v_pk_add_f32 v[172:173], v[172:173], 1.0 op_sel_hi:[1,0]
	v_pk_add_f32 v[174:175], v[174:175], 1.0 op_sel_hi:[1,0]
	v_pk_add_f32 v[176:177], v[176:177], 1.0 op_sel_hi:[1,0]
	v_pk_add_f32 v[180:181], v[180:181], 1.0 op_sel_hi:[1,0]
	v_rcp_f32_e32 v134, v172
	v_rcp_f32_e32 v135, v173
	v_rcp_f32_e32 v136, v174
	v_rcp_f32_e32 v137, v175
	v_rcp_f32_e32 v130, v176
	v_rcp_f32_e32 v131, v177
	v_rcp_f32_e32 v132, v180
	v_rcp_f32_e32 v133, v181
	v_pk_add_f32 v[126:127], v[126:127], v[14:15]
	v_pk_add_f32 v[128:129], v[128:129], v[16:17]
	v_pk_add_f32 v[122:123], v[122:123], v[10:11]
	v_pk_add_f32 v[124:125], v[124:125], v[12:13]
	v_pk_mul_f32 v[172:173], v[126:127], s[30:31] op_sel_hi:[1,0]
	v_pk_mul_f32 v[174:175], v[128:129], s[30:31] op_sel_hi:[1,0]
	v_pk_mul_f32 v[176:177], v[122:123], s[30:31] op_sel_hi:[1,0]
	v_pk_mul_f32 v[180:181], v[124:125], s[30:31] op_sel_hi:[1,0]
	v_exp_f32_e32 v172, v172
	v_exp_f32_e32 v173, v173
	v_exp_f32_e32 v174, v174
	v_exp_f32_e32 v175, v175
	v_exp_f32_e32 v176, v176
	v_exp_f32_e32 v177, v177
	v_exp_f32_e32 v180, v180
	v_exp_f32_e32 v181, v181
	v_pk_add_f32 v[172:173], v[172:173], 1.0 op_sel_hi:[1,0]
	v_pk_add_f32 v[174:175], v[174:175], 1.0 op_sel_hi:[1,0]
	v_pk_add_f32 v[176:177], v[176:177], 1.0 op_sel_hi:[1,0]
	v_pk_add_f32 v[180:181], v[180:181], 1.0 op_sel_hi:[1,0]
	v_rcp_f32_e32 v126, v172
	v_rcp_f32_e32 v127, v173
	v_rcp_f32_e32 v128, v174
	v_rcp_f32_e32 v129, v175
	v_rcp_f32_e32 v122, v176
	v_rcp_f32_e32 v123, v177
	v_rcp_f32_e32 v124, v180
	v_rcp_f32_e32 v125, v181
	v_pk_add_f32 v[118:119], v[118:119], v[6:7]
	v_pk_add_f32 v[120:121], v[120:121], v[8:9]
	v_pk_add_f32 v[114:115], v[114:115], v[2:3]
	v_pk_add_f32 v[116:117], v[116:117], v[4:5]
	v_pk_mul_f32 v[172:173], v[118:119], s[30:31] op_sel_hi:[1,0]
	v_pk_mul_f32 v[174:175], v[120:121], s[30:31] op_sel_hi:[1,0]
	v_pk_mul_f32 v[176:177], v[114:115], s[30:31] op_sel_hi:[1,0]
	v_pk_mul_f32 v[180:181], v[116:117], s[30:31] op_sel_hi:[1,0]
	v_exp_f32_e32 v172, v172
	v_exp_f32_e32 v173, v173
	v_exp_f32_e32 v174, v174
	v_exp_f32_e32 v175, v175
	v_exp_f32_e32 v176, v176
	v_exp_f32_e32 v177, v177
	v_exp_f32_e32 v180, v180
	v_exp_f32_e32 v181, v181
	v_pk_add_f32 v[172:173], v[172:173], 1.0 op_sel_hi:[1,0]
	v_pk_add_f32 v[174:175], v[174:175], 1.0 op_sel_hi:[1,0]
	v_pk_add_f32 v[176:177], v[176:177], 1.0 op_sel_hi:[1,0]
	v_pk_add_f32 v[180:181], v[180:181], 1.0 op_sel_hi:[1,0]
	v_rcp_f32_e32 v118, v172
	v_rcp_f32_e32 v119, v173
	v_rcp_f32_e32 v120, v174
	v_rcp_f32_e32 v121, v175
	v_rcp_f32_e32 v114, v176
	v_rcp_f32_e32 v115, v177
	v_rcp_f32_e32 v116, v180
	v_rcp_f32_e32 v117, v181
	v_pk_add_f32 v[110:111], v[110:111], v[14:15]
	v_pk_add_f32 v[112:113], v[112:113], v[16:17]
	v_pk_add_f32 v[106:107], v[106:107], v[10:11]
	v_pk_add_f32 v[108:109], v[108:109], v[12:13]
	v_pk_mul_f32 v[172:173], v[110:111], s[30:31] op_sel_hi:[1,0]
	v_pk_mul_f32 v[174:175], v[112:113], s[30:31] op_sel_hi:[1,0]
	v_pk_mul_f32 v[176:177], v[106:107], s[30:31] op_sel_hi:[1,0]
	v_pk_mul_f32 v[180:181], v[108:109], s[30:31] op_sel_hi:[1,0]
	v_exp_f32_e32 v172, v172
	v_exp_f32_e32 v173, v173
	v_exp_f32_e32 v174, v174
	v_exp_f32_e32 v175, v175
	v_exp_f32_e32 v176, v176
	v_exp_f32_e32 v177, v177
	v_exp_f32_e32 v180, v180
	v_exp_f32_e32 v181, v181
	v_pk_add_f32 v[172:173], v[172:173], 1.0 op_sel_hi:[1,0]
	v_pk_add_f32 v[174:175], v[174:175], 1.0 op_sel_hi:[1,0]
	v_pk_add_f32 v[176:177], v[176:177], 1.0 op_sel_hi:[1,0]
	v_pk_add_f32 v[180:181], v[180:181], 1.0 op_sel_hi:[1,0]
	v_rcp_f32_e32 v110, v172
	v_rcp_f32_e32 v111, v173
	v_rcp_f32_e32 v112, v174
	v_rcp_f32_e32 v113, v175
	v_rcp_f32_e32 v106, v176
	v_rcp_f32_e32 v107, v177
	v_rcp_f32_e32 v108, v180
	v_rcp_f32_e32 v109, v181
	v_pk_add_f32 v[102:103], v[102:103], v[6:7]
	v_pk_add_f32 v[104:105], v[104:105], v[8:9]
	v_pk_add_f32 v[98:99], v[98:99], v[2:3]
	v_pk_add_f32 v[100:101], v[100:101], v[4:5]
	v_pk_mul_f32 v[172:173], v[102:103], s[30:31] op_sel_hi:[1,0]
	v_pk_mul_f32 v[174:175], v[104:105], s[30:31] op_sel_hi:[1,0]
	v_pk_mul_f32 v[176:177], v[98:99], s[30:31] op_sel_hi:[1,0]
	v_pk_mul_f32 v[180:181], v[100:101], s[30:31] op_sel_hi:[1,0]
	v_exp_f32_e32 v172, v172
	v_exp_f32_e32 v173, v173
	v_exp_f32_e32 v174, v174
	v_exp_f32_e32 v175, v175
	v_exp_f32_e32 v176, v176
	v_exp_f32_e32 v177, v177
	v_exp_f32_e32 v180, v180
	v_exp_f32_e32 v181, v181
	v_pk_add_f32 v[172:173], v[172:173], 1.0 op_sel_hi:[1,0]
	v_pk_add_f32 v[174:175], v[174:175], 1.0 op_sel_hi:[1,0]
	v_pk_add_f32 v[176:177], v[176:177], 1.0 op_sel_hi:[1,0]
	v_pk_add_f32 v[180:181], v[180:181], 1.0 op_sel_hi:[1,0]
	v_rcp_f32_e32 v102, v172
	v_rcp_f32_e32 v103, v173
	v_rcp_f32_e32 v104, v174
	v_rcp_f32_e32 v105, v175
	v_rcp_f32_e32 v98, v176
	v_rcp_f32_e32 v99, v177
	v_rcp_f32_e32 v100, v180
	v_rcp_f32_e32 v101, v181
	v_pk_add_f32 v[94:95], v[94:95], v[14:15]
	v_pk_add_f32 v[96:97], v[96:97], v[16:17]
	v_pk_add_f32 v[90:91], v[90:91], v[10:11]
	v_pk_add_f32 v[92:93], v[92:93], v[12:13]
	v_pk_mul_f32 v[172:173], v[94:95], s[30:31] op_sel_hi:[1,0]
	v_pk_mul_f32 v[174:175], v[96:97], s[30:31] op_sel_hi:[1,0]
	v_pk_mul_f32 v[176:177], v[90:91], s[30:31] op_sel_hi:[1,0]
	v_pk_mul_f32 v[180:181], v[92:93], s[30:31] op_sel_hi:[1,0]
	v_exp_f32_e32 v172, v172
	v_exp_f32_e32 v173, v173
	v_exp_f32_e32 v174, v174
	v_exp_f32_e32 v175, v175
	v_exp_f32_e32 v176, v176
	v_exp_f32_e32 v177, v177
	v_exp_f32_e32 v180, v180
	v_exp_f32_e32 v181, v181
	v_pk_add_f32 v[172:173], v[172:173], 1.0 op_sel_hi:[1,0]
	v_pk_add_f32 v[174:175], v[174:175], 1.0 op_sel_hi:[1,0]
	v_pk_add_f32 v[176:177], v[176:177], 1.0 op_sel_hi:[1,0]
	v_pk_add_f32 v[180:181], v[180:181], 1.0 op_sel_hi:[1,0]
	v_rcp_f32_e32 v94, v172
	v_rcp_f32_e32 v95, v173
	v_rcp_f32_e32 v96, v174
	v_rcp_f32_e32 v97, v175
	v_rcp_f32_e32 v90, v176
	v_rcp_f32_e32 v91, v177
	v_rcp_f32_e32 v92, v180
	v_rcp_f32_e32 v93, v181
	v_pk_add_f32 v[86:87], v[86:87], v[6:7]
	v_pk_add_f32 v[88:89], v[88:89], v[8:9]
	v_pk_add_f32 v[82:83], v[82:83], v[2:3]
	v_pk_add_f32 v[84:85], v[84:85], v[4:5]
	v_pk_mul_f32 v[172:173], v[86:87], s[30:31] op_sel_hi:[1,0]
	v_pk_mul_f32 v[174:175], v[88:89], s[30:31] op_sel_hi:[1,0]
	v_pk_mul_f32 v[176:177], v[82:83], s[30:31] op_sel_hi:[1,0]
	v_pk_mul_f32 v[180:181], v[84:85], s[30:31] op_sel_hi:[1,0]
	v_exp_f32_e32 v172, v172
	v_exp_f32_e32 v173, v173
	v_exp_f32_e32 v174, v174
	v_exp_f32_e32 v175, v175
	v_exp_f32_e32 v176, v176
	v_exp_f32_e32 v177, v177
	v_exp_f32_e32 v180, v180
	v_exp_f32_e32 v181, v181
	v_pk_add_f32 v[172:173], v[172:173], 1.0 op_sel_hi:[1,0]
	v_pk_add_f32 v[174:175], v[174:175], 1.0 op_sel_hi:[1,0]
	v_pk_add_f32 v[176:177], v[176:177], 1.0 op_sel_hi:[1,0]
	v_pk_add_f32 v[180:181], v[180:181], 1.0 op_sel_hi:[1,0]
	v_rcp_f32_e32 v86, v172
	v_rcp_f32_e32 v87, v173
	v_rcp_f32_e32 v88, v174
	v_rcp_f32_e32 v89, v175
	v_rcp_f32_e32 v82, v176
	v_rcp_f32_e32 v83, v177
	v_rcp_f32_e32 v84, v180
	v_rcp_f32_e32 v85, v181
	v_pk_add_f32 v[78:79], v[78:79], v[14:15]
	v_pk_add_f32 v[80:81], v[80:81], v[16:17]
	v_pk_add_f32 v[74:75], v[74:75], v[10:11]
	v_pk_add_f32 v[76:77], v[76:77], v[12:13]
	v_pk_mul_f32 v[172:173], v[78:79], s[30:31] op_sel_hi:[1,0]
	v_pk_mul_f32 v[174:175], v[80:81], s[30:31] op_sel_hi:[1,0]
	v_pk_mul_f32 v[176:177], v[74:75], s[30:31] op_sel_hi:[1,0]
	v_pk_mul_f32 v[180:181], v[76:77], s[30:31] op_sel_hi:[1,0]
	v_exp_f32_e32 v172, v172
	v_exp_f32_e32 v173, v173
	v_exp_f32_e32 v174, v174
	v_exp_f32_e32 v175, v175
	v_exp_f32_e32 v176, v176
	v_exp_f32_e32 v177, v177
	v_exp_f32_e32 v180, v180
	v_exp_f32_e32 v181, v181
	v_pk_add_f32 v[172:173], v[172:173], 1.0 op_sel_hi:[1,0]
	v_pk_add_f32 v[174:175], v[174:175], 1.0 op_sel_hi:[1,0]
	v_pk_add_f32 v[176:177], v[176:177], 1.0 op_sel_hi:[1,0]
	v_pk_add_f32 v[180:181], v[180:181], 1.0 op_sel_hi:[1,0]
	v_rcp_f32_e32 v78, v172
	v_rcp_f32_e32 v79, v173
	v_rcp_f32_e32 v80, v174
	v_rcp_f32_e32 v81, v175
	v_rcp_f32_e32 v74, v176
	v_rcp_f32_e32 v75, v177
	v_rcp_f32_e32 v76, v180
	v_rcp_f32_e32 v77, v181
	v_pk_add_f32 v[70:71], v[70:71], v[6:7]
	v_pk_add_f32 v[72:73], v[72:73], v[8:9]
	v_pk_add_f32 v[66:67], v[66:67], v[2:3]
	v_pk_add_f32 v[68:69], v[68:69], v[4:5]
	v_pk_mul_f32 v[172:173], v[70:71], s[30:31] op_sel_hi:[1,0]
	v_pk_mul_f32 v[174:175], v[72:73], s[30:31] op_sel_hi:[1,0]
	v_pk_mul_f32 v[176:177], v[66:67], s[30:31] op_sel_hi:[1,0]
	v_pk_mul_f32 v[180:181], v[68:69], s[30:31] op_sel_hi:[1,0]
	v_exp_f32_e32 v172, v172
	v_exp_f32_e32 v173, v173
	v_exp_f32_e32 v174, v174
	v_exp_f32_e32 v175, v175
	v_exp_f32_e32 v176, v176
	v_exp_f32_e32 v177, v177
	v_exp_f32_e32 v180, v180
	v_exp_f32_e32 v181, v181
	v_pk_add_f32 v[172:173], v[172:173], 1.0 op_sel_hi:[1,0]
	v_pk_add_f32 v[174:175], v[174:175], 1.0 op_sel_hi:[1,0]
	v_pk_add_f32 v[176:177], v[176:177], 1.0 op_sel_hi:[1,0]
	v_pk_add_f32 v[180:181], v[180:181], 1.0 op_sel_hi:[1,0]
	v_rcp_f32_e32 v70, v172
	v_rcp_f32_e32 v71, v173
	v_rcp_f32_e32 v72, v174
	v_rcp_f32_e32 v73, v175
	v_rcp_f32_e32 v66, v176
	v_rcp_f32_e32 v67, v177
	v_rcp_f32_e32 v68, v180
	v_rcp_f32_e32 v69, v181
	v_pk_add_f32 v[62:63], v[62:63], v[14:15]
	v_pk_add_f32 v[64:65], v[64:65], v[16:17]
	v_pk_add_f32 v[58:59], v[58:59], v[10:11]
	v_pk_add_f32 v[60:61], v[60:61], v[12:13]
	v_pk_mul_f32 v[172:173], v[62:63], s[30:31] op_sel_hi:[1,0]
	v_pk_mul_f32 v[174:175], v[64:65], s[30:31] op_sel_hi:[1,0]
	v_pk_mul_f32 v[176:177], v[58:59], s[30:31] op_sel_hi:[1,0]
	v_pk_mul_f32 v[180:181], v[60:61], s[30:31] op_sel_hi:[1,0]
	v_exp_f32_e32 v172, v172
	v_exp_f32_e32 v173, v173
	v_exp_f32_e32 v174, v174
	v_exp_f32_e32 v175, v175
	v_exp_f32_e32 v176, v176
	v_exp_f32_e32 v177, v177
	v_exp_f32_e32 v180, v180
	v_exp_f32_e32 v181, v181
	v_pk_add_f32 v[172:173], v[172:173], 1.0 op_sel_hi:[1,0]
	v_pk_add_f32 v[174:175], v[174:175], 1.0 op_sel_hi:[1,0]
	v_pk_add_f32 v[176:177], v[176:177], 1.0 op_sel_hi:[1,0]
	v_pk_add_f32 v[180:181], v[180:181], 1.0 op_sel_hi:[1,0]
	v_rcp_f32_e32 v62, v172
	v_rcp_f32_e32 v63, v173
	v_rcp_f32_e32 v64, v174
	v_rcp_f32_e32 v65, v175
	v_rcp_f32_e32 v58, v176
	v_rcp_f32_e32 v59, v177
	v_rcp_f32_e32 v60, v180
	v_rcp_f32_e32 v61, v181
	v_pk_add_f32 v[54:55], v[54:55], v[6:7]
	v_pk_add_f32 v[56:57], v[56:57], v[8:9]
	v_pk_add_f32 v[50:51], v[50:51], v[2:3]
	v_pk_add_f32 v[52:53], v[52:53], v[4:5]
	v_pk_mul_f32 v[172:173], v[54:55], s[30:31] op_sel_hi:[1,0]
	v_pk_mul_f32 v[174:175], v[56:57], s[30:31] op_sel_hi:[1,0]
	v_pk_mul_f32 v[176:177], v[50:51], s[30:31] op_sel_hi:[1,0]
	v_pk_mul_f32 v[180:181], v[52:53], s[30:31] op_sel_hi:[1,0]
	v_exp_f32_e32 v172, v172
	v_exp_f32_e32 v173, v173
	v_exp_f32_e32 v174, v174
	v_exp_f32_e32 v175, v175
	v_exp_f32_e32 v176, v176
	v_exp_f32_e32 v177, v177
	v_exp_f32_e32 v180, v180
	v_exp_f32_e32 v181, v181
	v_pk_add_f32 v[172:173], v[172:173], 1.0 op_sel_hi:[1,0]
	v_pk_add_f32 v[174:175], v[174:175], 1.0 op_sel_hi:[1,0]
	v_pk_add_f32 v[176:177], v[176:177], 1.0 op_sel_hi:[1,0]
	v_pk_add_f32 v[180:181], v[180:181], 1.0 op_sel_hi:[1,0]
	v_rcp_f32_e32 v54, v172
	v_rcp_f32_e32 v55, v173
	v_rcp_f32_e32 v56, v174
	v_rcp_f32_e32 v57, v175
	v_rcp_f32_e32 v50, v176
	v_rcp_f32_e32 v51, v177
	v_rcp_f32_e32 v52, v180
	v_rcp_f32_e32 v53, v181
	v_pk_add_f32 v[46:47], v[46:47], v[14:15]
	v_pk_add_f32 v[48:49], v[48:49], v[16:17]
	v_pk_add_f32 v[42:43], v[42:43], v[10:11]
	v_pk_add_f32 v[44:45], v[44:45], v[12:13]
	v_pk_mul_f32 v[172:173], v[46:47], s[30:31] op_sel_hi:[1,0]
	v_pk_mul_f32 v[174:175], v[48:49], s[30:31] op_sel_hi:[1,0]
	v_pk_mul_f32 v[176:177], v[42:43], s[30:31] op_sel_hi:[1,0]
	v_pk_mul_f32 v[180:181], v[44:45], s[30:31] op_sel_hi:[1,0]
	v_exp_f32_e32 v172, v172
	v_exp_f32_e32 v173, v173
	v_exp_f32_e32 v174, v174
	v_exp_f32_e32 v175, v175
	v_exp_f32_e32 v176, v176
	v_exp_f32_e32 v177, v177
	v_exp_f32_e32 v180, v180
	v_exp_f32_e32 v181, v181
	v_pk_add_f32 v[172:173], v[172:173], 1.0 op_sel_hi:[1,0]
	v_pk_add_f32 v[174:175], v[174:175], 1.0 op_sel_hi:[1,0]
	v_pk_add_f32 v[176:177], v[176:177], 1.0 op_sel_hi:[1,0]
	v_pk_add_f32 v[180:181], v[180:181], 1.0 op_sel_hi:[1,0]
	v_rcp_f32_e32 v46, v172
	v_rcp_f32_e32 v47, v173
	v_rcp_f32_e32 v48, v174
	v_rcp_f32_e32 v49, v175
	v_rcp_f32_e32 v42, v176
	v_rcp_f32_e32 v43, v177
	v_rcp_f32_e32 v44, v180
	v_rcp_f32_e32 v45, v181
	v_pk_add_f32 v[38:39], v[38:39], v[6:7]
	v_pk_add_f32 v[40:41], v[40:41], v[8:9]
	v_pk_add_f32 v[34:35], v[34:35], v[2:3]
	v_pk_add_f32 v[36:37], v[36:37], v[4:5]
	v_pk_mul_f32 v[172:173], v[38:39], s[30:31] op_sel_hi:[1,0]
	v_pk_mul_f32 v[174:175], v[40:41], s[30:31] op_sel_hi:[1,0]
	v_pk_mul_f32 v[176:177], v[34:35], s[30:31] op_sel_hi:[1,0]
	v_pk_mul_f32 v[180:181], v[36:37], s[30:31] op_sel_hi:[1,0]
	v_exp_f32_e32 v172, v172
	v_exp_f32_e32 v173, v173
	v_exp_f32_e32 v174, v174
	v_exp_f32_e32 v175, v175
	v_exp_f32_e32 v176, v176
	v_exp_f32_e32 v177, v177
	v_exp_f32_e32 v180, v180
	v_exp_f32_e32 v181, v181
	v_pk_add_f32 v[172:173], v[172:173], 1.0 op_sel_hi:[1,0]
	v_pk_add_f32 v[174:175], v[174:175], 1.0 op_sel_hi:[1,0]
	v_pk_add_f32 v[176:177], v[176:177], 1.0 op_sel_hi:[1,0]
	v_pk_add_f32 v[180:181], v[180:181], 1.0 op_sel_hi:[1,0]
	v_rcp_f32_e32 v38, v172
	v_rcp_f32_e32 v39, v173
	v_rcp_f32_e32 v40, v174
	v_rcp_f32_e32 v41, v175
	v_rcp_f32_e32 v34, v176
	v_rcp_f32_e32 v35, v177
	v_rcp_f32_e32 v36, v180
	v_rcp_f32_e32 v37, v181
	v_mov_b32_e32 v2, 0
	v_mov_b32_e32 v3, 0
	v_mov_b32_e32 v4, 0
	v_mov_b32_e32 v5, 0
	v_mov_b32_e32 v6, 0
	v_mov_b32_e32 v7, 0
	v_mov_b32_e32 v8, 0
	v_mov_b32_e32 v9, 0
	s_and_b64 vcc, exec, s[0:1]
	s_cbranch_vccnz .Lmg_m0
	v_mov_b32_e32 v2, v224
	v_mov_b32_e32 v3, v225
	v_mov_b32_e32 v4, v226
	v_mov_b32_e32 v5, v227
	v_mov_b32_e32 v6, v228
	v_mov_b32_e32 v7, v229
	v_mov_b32_e32 v8, v230
	v_mov_b32_e32 v9, v231
.Lmg_m0:
	v_mov_b32_e32 v10, 0
	v_mov_b32_e32 v11, 0
	v_mov_b32_e32 v12, 0
	v_mov_b32_e32 v13, 0
	v_mov_b32_e32 v14, 0
	v_mov_b32_e32 v15, 0
	v_mov_b32_e32 v16, 0
	v_mov_b32_e32 v17, 0
	s_and_b64 vcc, exec, s[0:1]
	s_cbranch_vccnz .Lmg_m1
	v_mov_b32_e32 v10, v232
	v_mov_b32_e32 v11, v233
	v_mov_b32_e32 v12, v234
	v_mov_b32_e32 v13, v235
	v_mov_b32_e32 v14, v236
	v_mov_b32_e32 v15, v237
	v_mov_b32_e32 v16, v238
	v_mov_b32_e32 v17, v239
.Lmg_m1:
	s_waitcnt vmcnt(2)
	v_lshlrev_b32_e32 v172, 16, v24
	v_and_b32_e32 v173, 0xffff0000, v24
	v_lshlrev_b32_e32 v174, 16, v2
	v_and_b32_e32 v175, 0xffff0000, v2
	v_pk_fma_f32 v[158:159], v[158:159], v[172:173], v[174:175]
	v_lshlrev_b32_e32 v176, 16, v25
	v_and_b32_e32 v177, 0xffff0000, v25
	v_lshlrev_b32_e32 v180, 16, v3
	v_and_b32_e32 v181, 0xffff0000, v3
	v_pk_fma_f32 v[160:161], v[160:161], v[176:177], v[180:181]
	v_lshlrev_b32_e32 v172, 16, v26
	v_and_b32_e32 v173, 0xffff0000, v26
	v_lshlrev_b32_e32 v174, 16, v4
	v_and_b32_e32 v175, 0xffff0000, v4
	v_pk_fma_f32 v[154:155], v[154:155], v[172:173], v[174:175]
	v_lshlrev_b32_e32 v176, 16, v27
	v_and_b32_e32 v177, 0xffff0000, v27
	v_lshlrev_b32_e32 v180, 16, v5
	v_and_b32_e32 v181, 0xffff0000, v5
	v_pk_fma_f32 v[156:157], v[156:157], v[176:177], v[180:181]
	v_cvt_pk_bf16_f32 v194, v158, v159
	v_cvt_pk_bf16_f32 v195, v160, v161
	v_cvt_pk_bf16_f32 v196, v154, v155
	v_cvt_pk_bf16_f32 v197, v156, v157
	s_mov_b32 s36, 0x0
	v_lshl_add_u64 v[22:23], v[20:21], 0, s[36:37]
	v_mov_b32_e32 v224, v194
	v_mov_b32_e32 v225, v195
	v_mov_b32_e32 v226, v196
	v_mov_b32_e32 v227, v197
	s_mov_b64 exec, s[34:35]
	global_store_dwordx4 v[22:23], v[194:197], off
	s_mov_b64 exec, -1
	s_nop 1
	v_lshlrev_b32_e32 v172, 16, v28
	v_and_b32_e32 v173, 0xffff0000, v28
	v_lshlrev_b32_e32 v174, 16, v6
	v_and_b32_e32 v175, 0xffff0000, v6
	v_pk_fma_f32 v[150:151], v[150:151], v[172:173], v[174:175]
	v_lshlrev_b32_e32 v176, 16, v29
	v_and_b32_e32 v177, 0xffff0000, v29
	v_lshlrev_b32_e32 v180, 16, v7
	v_and_b32_e32 v181, 0xffff0000, v7
	v_pk_fma_f32 v[152:153], v[152:153], v[176:177], v[180:181]
	v_lshlrev_b32_e32 v172, 16, v30
	v_and_b32_e32 v173, 0xffff0000, v30
	v_lshlrev_b32_e32 v174, 16, v8
	v_and_b32_e32 v175, 0xffff0000, v8
	v_pk_fma_f32 v[146:147], v[146:147], v[172:173], v[174:175]
	v_lshlrev_b32_e32 v176, 16, v31
	v_and_b32_e32 v177, 0xffff0000, v31
	v_lshlrev_b32_e32 v180, 16, v9
	v_and_b32_e32 v181, 0xffff0000, v9
	v_pk_fma_f32 v[148:149], v[148:149], v[176:177], v[180:181]
	v_cvt_pk_bf16_f32 v194, v150, v151
	v_cvt_pk_bf16_f32 v195, v152, v153
	v_cvt_pk_bf16_f32 v196, v146, v147
	v_cvt_pk_bf16_f32 v197, v148, v149
	v_mov_b32_e32 v228, v194
	v_mov_b32_e32 v229, v195
	v_mov_b32_e32 v230, v196
	v_mov_b32_e32 v231, v197
	s_mov_b64 exec, s[34:35]
	global_store_dwordx4 v[22:23], v[194:197], off offset:256
	s_mov_b64 exec, -1
	s_nop 1
	s_mov_b32 s36, 0x30000
	v_lshl_add_u64 v[22:23], v[18:19], 0, s[36:37]
	global_load_dwordx4 v[24:27], v[22:23], off
	global_load_dwordx4 v[28:31], v[22:23], off offset:256
	v_mov_b32_e32 v2, 0
	v_mov_b32_e32 v3, 0
	v_mov_b32_e32 v4, 0
	v_mov_b32_e32 v5, 0
	v_mov_b32_e32 v6, 0
	v_mov_b32_e32 v7, 0
	v_mov_b32_e32 v8, 0
	v_mov_b32_e32 v9, 0
	s_and_b64 vcc, exec, s[0:1]
	s_cbranch_vccnz .Lmg_m2
	v_mov_b32_e32 v2, v240
	v_mov_b32_e32 v3, v241
	v_mov_b32_e32 v4, v246
	v_mov_b32_e32 v5, v247
	v_mov_b32_e32 v6, v248
	v_mov_b32_e32 v7, v249
	v_mov_b32_e32 v8, v216
	v_mov_b32_e32 v9, v217
.Lmg_m2:
	s_waitcnt vmcnt(4)
	v_lshlrev_b32_e32 v172, 16, v164
	v_and_b32_e32 v173, 0xffff0000, v164
	v_lshlrev_b32_e32 v174, 16, v10
	v_and_b32_e32 v175, 0xffff0000, v10
	v_pk_fma_f32 v[142:143], v[142:143], v[172:173], v[174:175]
	v_lshlrev_b32_e32 v176, 16, v165
	v_and_b32_e32 v177, 0xffff0000, v165
	v_lshlrev_b32_e32 v180, 16, v11
	v_and_b32_e32 v181, 0xffff0000, v11
	v_pk_fma_f32 v[144:145], v[144:145], v[176:177], v[180:181]
	v_lshlrev_b32_e32 v172, 16, v166
	v_and_b32_e32 v173, 0xffff0000, v166
	v_lshlrev_b32_e32 v174, 16, v12
	v_and_b32_e32 v175, 0xffff0000, v12
	v_pk_fma_f32 v[138:139], v[138:139], v[172:173], v[174:175]
	v_lshlrev_b32_e32 v176, 16, v167
	v_and_b32_e32 v177, 0xffff0000, v167
	v_lshlrev_b32_e32 v180, 16, v13
	v_and_b32_e32 v181, 0xffff0000, v13
	v_pk_fma_f32 v[140:141], v[140:141], v[176:177], v[180:181]
	v_cvt_pk_bf16_f32 v194, v142, v143
	v_cvt_pk_bf16_f32 v195, v144, v145
	v_cvt_pk_bf16_f32 v196, v138, v139
	v_cvt_pk_bf16_f32 v197, v140, v141
	s_mov_b32 s36, 0x8000
	v_lshl_add_u64 v[22:23], v[20:21], 0, s[36:37]
	v_mov_b32_e32 v232, v194
	v_mov_b32_e32 v233, v195
	v_mov_b32_e32 v234, v196
	v_mov_b32_e32 v235, v197
	s_mov_b64 exec, s[34:35]
	global_store_dwordx4 v[22:23], v[194:197], off
	s_mov_b64 exec, -1
	s_nop 1
	v_lshlrev_b32_e32 v172, 16, v168
	v_and_b32_e32 v173, 0xffff0000, v168
	v_lshlrev_b32_e32 v174, 16, v14
	v_and_b32_e32 v175, 0xffff0000, v14
	v_pk_fma_f32 v[134:135], v[134:135], v[172:173], v[174:175]
	v_lshlrev_b32_e32 v176, 16, v169
	v_and_b32_e32 v177, 0xffff0000, v169
	v_lshlrev_b32_e32 v180, 16, v15
	v_and_b32_e32 v181, 0xffff0000, v15
	v_pk_fma_f32 v[136:137], v[136:137], v[176:177], v[180:181]
	v_lshlrev_b32_e32 v172, 16, v170
	v_and_b32_e32 v173, 0xffff0000, v170
	v_lshlrev_b32_e32 v174, 16, v16
	v_and_b32_e32 v175, 0xffff0000, v16
	v_pk_fma_f32 v[130:131], v[130:131], v[172:173], v[174:175]
	v_lshlrev_b32_e32 v176, 16, v171
	v_and_b32_e32 v177, 0xffff0000, v171
	v_lshlrev_b32_e32 v180, 16, v17
	v_and_b32_e32 v181, 0xffff0000, v17
	v_pk_fma_f32 v[132:133], v[132:133], v[176:177], v[180:181]
	v_cvt_pk_bf16_f32 v194, v134, v135
	v_cvt_pk_bf16_f32 v195, v136, v137
	v_cvt_pk_bf16_f32 v196, v130, v131
	v_cvt_pk_bf16_f32 v197, v132, v133
	v_mov_b32_e32 v236, v194
	v_mov_b32_e32 v237, v195
	v_mov_b32_e32 v238, v196
	v_mov_b32_e32 v239, v197
	s_mov_b64 exec, s[34:35]
	global_store_dwordx4 v[22:23], v[194:197], off offset:256
	s_mov_b64 exec, -1
	s_nop 1
	s_mov_b32 s36, 0x48000
	v_lshl_add_u64 v[22:23], v[18:19], 0, s[36:37]
	global_load_dwordx4 v[164:167], v[22:23], off
	global_load_dwordx4 v[168:171], v[22:23], off offset:256
	v_mov_b32_e32 v10, 0
	v_mov_b32_e32 v11, 0
	v_mov_b32_e32 v12, 0
	v_mov_b32_e32 v13, 0
	v_mov_b32_e32 v14, 0
	v_mov_b32_e32 v15, 0
	v_mov_b32_e32 v16, 0
	v_mov_b32_e32 v17, 0
	s_and_b64 vcc, exec, s[0:1]
	s_cbranch_vccnz .Lmg_m3
	v_mov_b32_e32 v10, v218
	v_mov_b32_e32 v11, v219
	v_mov_b32_e32 v12, v242
	v_mov_b32_e32 v13, v243
	v_mov_b32_e32 v14, v244
	v_mov_b32_e32 v15, v245
	v_mov_b32_e32 v16, v211
	v_mov_b32_e32 v17, v212
.Lmg_m3:
	s_waitcnt vmcnt(4)
	v_lshlrev_b32_e32 v172, 16, v24
	v_and_b32_e32 v173, 0xffff0000, v24
	v_lshlrev_b32_e32 v174, 16, v2
	v_and_b32_e32 v175, 0xffff0000, v2
	v_pk_fma_f32 v[126:127], v[126:127], v[172:173], v[174:175]
	v_lshlrev_b32_e32 v176, 16, v25
	v_and_b32_e32 v177, 0xffff0000, v25
	v_lshlrev_b32_e32 v180, 16, v3
	v_and_b32_e32 v181, 0xffff0000, v3
	v_pk_fma_f32 v[128:129], v[128:129], v[176:177], v[180:181]
	v_lshlrev_b32_e32 v172, 16, v26
	v_and_b32_e32 v173, 0xffff0000, v26
	v_lshlrev_b32_e32 v174, 16, v4
	v_and_b32_e32 v175, 0xffff0000, v4
	v_pk_fma_f32 v[122:123], v[122:123], v[172:173], v[174:175]
	v_lshlrev_b32_e32 v176, 16, v27
	v_and_b32_e32 v177, 0xffff0000, v27
	v_lshlrev_b32_e32 v180, 16, v5
	v_and_b32_e32 v181, 0xffff0000, v5
	v_pk_fma_f32 v[124:125], v[124:125], v[176:177], v[180:181]
	v_cvt_pk_bf16_f32 v194, v126, v127
	v_cvt_pk_bf16_f32 v195, v128, v129
	v_cvt_pk_bf16_f32 v196, v122, v123
	v_cvt_pk_bf16_f32 v197, v124, v125
	s_mov_b32 s36, 0x10000
	v_lshl_add_u64 v[22:23], v[20:21], 0, s[36:37]
	v_mov_b32_e32 v240, v194
	v_mov_b32_e32 v241, v195
	v_mov_b32_e32 v246, v196
	v_mov_b32_e32 v247, v197
	s_mov_b64 exec, s[34:35]
	global_store_dwordx4 v[22:23], v[194:197], off
	s_mov_b64 exec, -1
	s_nop 1
	v_lshlrev_b32_e32 v172, 16, v28
	v_and_b32_e32 v173, 0xffff0000, v28
	v_lshlrev_b32_e32 v174, 16, v6
	v_and_b32_e32 v175, 0xffff0000, v6
	v_pk_fma_f32 v[118:119], v[118:119], v[172:173], v[174:175]
	v_lshlrev_b32_e32 v176, 16, v29
	v_and_b32_e32 v177, 0xffff0000, v29
	v_lshlrev_b32_e32 v180, 16, v7
	v_and_b32_e32 v181, 0xffff0000, v7
	v_pk_fma_f32 v[120:121], v[120:121], v[176:177], v[180:181]
	v_lshlrev_b32_e32 v172, 16, v30
	v_and_b32_e32 v173, 0xffff0000, v30
	v_lshlrev_b32_e32 v174, 16, v8
	v_and_b32_e32 v175, 0xffff0000, v8
	v_pk_fma_f32 v[114:115], v[114:115], v[172:173], v[174:175]
	v_lshlrev_b32_e32 v176, 16, v31
	v_and_b32_e32 v177, 0xffff0000, v31
	v_lshlrev_b32_e32 v180, 16, v9
	v_and_b32_e32 v181, 0xffff0000, v9
	v_pk_fma_f32 v[116:117], v[116:117], v[176:177], v[180:181]
	v_cvt_pk_bf16_f32 v194, v118, v119
	v_cvt_pk_bf16_f32 v195, v120, v121
	v_cvt_pk_bf16_f32 v196, v114, v115
	v_cvt_pk_bf16_f32 v197, v116, v117
	v_mov_b32_e32 v248, v194
	v_mov_b32_e32 v249, v195
	v_mov_b32_e32 v216, v196
	v_mov_b32_e32 v217, v197
	s_mov_b64 exec, s[34:35]
	global_store_dwordx4 v[22:23], v[194:197], off offset:256
	s_mov_b64 exec, -1
	s_nop 1
	s_mov_b32 s36, 0xc0000
	v_lshl_add_u64 v[22:23], v[18:19], 0, s[36:37]
	global_load_dwordx4 v[24:27], v[22:23], off
	global_load_dwordx4 v[28:31], v[22:23], off offset:256
	v_mov_b32_e32 v2, 0
	v_mov_b32_e32 v3, 0
	v_mov_b32_e32 v4, 0
	v_mov_b32_e32 v5, 0
	v_mov_b32_e32 v6, 0
	v_mov_b32_e32 v7, 0
	v_mov_b32_e32 v8, 0
	v_mov_b32_e32 v9, 0
	s_and_b64 vcc, exec, s[0:1]
	s_cbranch_vccnz .Lmg_m4
	v_mov_b32_e32 v2, v214
	v_mov_b32_e32 v3, v215
	v_mov_b32_e32 v4, v220
	v_mov_b32_e32 v5, v221
	ds_read_b128 v[6:9], v222
	s_waitcnt lgkmcnt(0)
.Lmg_m4:
	s_waitcnt vmcnt(4)
	v_lshlrev_b32_e32 v172, 16, v164
	v_and_b32_e32 v173, 0xffff0000, v164
	v_lshlrev_b32_e32 v174, 16, v10
	v_and_b32_e32 v175, 0xffff0000, v10
	v_pk_fma_f32 v[110:111], v[110:111], v[172:173], v[174:175]
	v_lshlrev_b32_e32 v176, 16, v165
	v_and_b32_e32 v177, 0xffff0000, v165
	v_lshlrev_b32_e32 v180, 16, v11
	v_and_b32_e32 v181, 0xffff0000, v11
	v_pk_fma_f32 v[112:113], v[112:113], v[176:177], v[180:181]
	v_lshlrev_b32_e32 v172, 16, v166
	v_and_b32_e32 v173, 0xffff0000, v166
	v_lshlrev_b32_e32 v174, 16, v12
	v_and_b32_e32 v175, 0xffff0000, v12
	v_pk_fma_f32 v[106:107], v[106:107], v[172:173], v[174:175]
	v_lshlrev_b32_e32 v176, 16, v167
	v_and_b32_e32 v177, 0xffff0000, v167
	v_lshlrev_b32_e32 v180, 16, v13
	v_and_b32_e32 v181, 0xffff0000, v13
	v_pk_fma_f32 v[108:109], v[108:109], v[176:177], v[180:181]
	v_cvt_pk_bf16_f32 v194, v110, v111
	v_cvt_pk_bf16_f32 v195, v112, v113
	v_cvt_pk_bf16_f32 v196, v106, v107
	v_cvt_pk_bf16_f32 v197, v108, v109
	s_mov_b32 s36, 0x18000
	v_lshl_add_u64 v[22:23], v[20:21], 0, s[36:37]
	v_mov_b32_e32 v218, v194
	v_mov_b32_e32 v219, v195
	v_mov_b32_e32 v242, v196
	v_mov_b32_e32 v243, v197
	s_mov_b64 exec, s[34:35]
	global_store_dwordx4 v[22:23], v[194:197], off
	s_mov_b64 exec, -1
	s_nop 1
	v_lshlrev_b32_e32 v172, 16, v168
	v_and_b32_e32 v173, 0xffff0000, v168
	v_lshlrev_b32_e32 v174, 16, v14
	v_and_b32_e32 v175, 0xffff0000, v14
	v_pk_fma_f32 v[102:103], v[102:103], v[172:173], v[174:175]
	v_lshlrev_b32_e32 v176, 16, v169
	v_and_b32_e32 v177, 0xffff0000, v169
	v_lshlrev_b32_e32 v180, 16, v15
	v_and_b32_e32 v181, 0xffff0000, v15
	v_pk_fma_f32 v[104:105], v[104:105], v[176:177], v[180:181]
	v_lshlrev_b32_e32 v172, 16, v170
	v_and_b32_e32 v173, 0xffff0000, v170
	v_lshlrev_b32_e32 v174, 16, v16
	v_and_b32_e32 v175, 0xffff0000, v16
	v_pk_fma_f32 v[98:99], v[98:99], v[172:173], v[174:175]
	v_lshlrev_b32_e32 v176, 16, v171
	v_and_b32_e32 v177, 0xffff0000, v171
	v_lshlrev_b32_e32 v180, 16, v17
	v_and_b32_e32 v181, 0xffff0000, v17
	v_pk_fma_f32 v[100:101], v[100:101], v[176:177], v[180:181]
	v_cvt_pk_bf16_f32 v194, v102, v103
	v_cvt_pk_bf16_f32 v195, v104, v105
	v_cvt_pk_bf16_f32 v196, v98, v99
	v_cvt_pk_bf16_f32 v197, v100, v101
	v_mov_b32_e32 v244, v194
	v_mov_b32_e32 v245, v195
	v_mov_b32_e32 v211, v196
	v_mov_b32_e32 v212, v197
	s_mov_b64 exec, s[34:35]
	global_store_dwordx4 v[22:23], v[194:197], off offset:256
	s_mov_b64 exec, -1
	s_nop 1
	s_mov_b32 s36, 0xd8000
	v_lshl_add_u64 v[22:23], v[18:19], 0, s[36:37]
	global_load_dwordx4 v[164:167], v[22:23], off
	global_load_dwordx4 v[168:171], v[22:23], off offset:256
	v_mov_b32_e32 v10, 0
	v_mov_b32_e32 v11, 0
	v_mov_b32_e32 v12, 0
	v_mov_b32_e32 v13, 0
	v_mov_b32_e32 v14, 0
	v_mov_b32_e32 v15, 0
	v_mov_b32_e32 v16, 0
	v_mov_b32_e32 v17, 0
	s_and_b64 vcc, exec, s[0:1]
	s_cbranch_vccnz .Lmg_m5
	ds_read_b128 v[10:13], v222 offset:16192
	ds_read_b128 v[14:17], v222 offset:24384
	s_waitcnt lgkmcnt(0)
.Lmg_m5:
	s_waitcnt vmcnt(4)
	v_lshlrev_b32_e32 v172, 16, v24
	v_and_b32_e32 v173, 0xffff0000, v24
	v_lshlrev_b32_e32 v174, 16, v2
	v_and_b32_e32 v175, 0xffff0000, v2
	v_pk_fma_f32 v[94:95], v[94:95], v[172:173], v[174:175]
	v_lshlrev_b32_e32 v176, 16, v25
	v_and_b32_e32 v177, 0xffff0000, v25
	v_lshlrev_b32_e32 v180, 16, v3
	v_and_b32_e32 v181, 0xffff0000, v3
	v_pk_fma_f32 v[96:97], v[96:97], v[176:177], v[180:181]
	v_lshlrev_b32_e32 v172, 16, v26
	v_and_b32_e32 v173, 0xffff0000, v26
	v_lshlrev_b32_e32 v174, 16, v4
	v_and_b32_e32 v175, 0xffff0000, v4
	v_pk_fma_f32 v[90:91], v[90:91], v[172:173], v[174:175]
	v_lshlrev_b32_e32 v176, 16, v27
	v_and_b32_e32 v177, 0xffff0000, v27
	v_lshlrev_b32_e32 v180, 16, v5
	v_and_b32_e32 v181, 0xffff0000, v5
	v_pk_fma_f32 v[92:93], v[92:93], v[176:177], v[180:181]
	v_cvt_pk_bf16_f32 v194, v94, v95
	v_cvt_pk_bf16_f32 v195, v96, v97
	v_cvt_pk_bf16_f32 v196, v90, v91
	v_cvt_pk_bf16_f32 v197, v92, v93
	s_mov_b32 s36, 0x40000
	v_lshl_add_u64 v[22:23], v[20:21], 0, s[36:37]
	v_mov_b32_e32 v214, v194
	v_mov_b32_e32 v215, v195
	v_mov_b32_e32 v220, v196
	v_mov_b32_e32 v221, v197
	s_mov_b64 exec, s[34:35]
	global_store_dwordx4 v[22:23], v[194:197], off
	s_mov_b64 exec, -1
	s_nop 1
	v_lshlrev_b32_e32 v172, 16, v28
	v_and_b32_e32 v173, 0xffff0000, v28
	v_lshlrev_b32_e32 v174, 16, v6
	v_and_b32_e32 v175, 0xffff0000, v6
	v_pk_fma_f32 v[86:87], v[86:87], v[172:173], v[174:175]
	v_lshlrev_b32_e32 v176, 16, v29
	v_and_b32_e32 v177, 0xffff0000, v29
	v_lshlrev_b32_e32 v180, 16, v7
	v_and_b32_e32 v181, 0xffff0000, v7
	v_pk_fma_f32 v[88:89], v[88:89], v[176:177], v[180:181]
	v_lshlrev_b32_e32 v172, 16, v30
	v_and_b32_e32 v173, 0xffff0000, v30
	v_lshlrev_b32_e32 v174, 16, v8
	v_and_b32_e32 v175, 0xffff0000, v8
	v_pk_fma_f32 v[82:83], v[82:83], v[172:173], v[174:175]
	v_lshlrev_b32_e32 v176, 16, v31
	v_and_b32_e32 v177, 0xffff0000, v31
	v_lshlrev_b32_e32 v180, 16, v9
	v_and_b32_e32 v181, 0xffff0000, v9
	v_pk_fma_f32 v[84:85], v[84:85], v[176:177], v[180:181]
	v_cvt_pk_bf16_f32 v194, v86, v87
	v_cvt_pk_bf16_f32 v195, v88, v89
	v_cvt_pk_bf16_f32 v196, v82, v83
	v_cvt_pk_bf16_f32 v197, v84, v85
	ds_write_b128 v222, v[194:197]
	s_mov_b64 exec, s[34:35]
	global_store_dwordx4 v[22:23], v[194:197], off offset:256
	s_mov_b64 exec, -1
	s_nop 1
	s_mov_b32 s36, 0xf0000
	v_lshl_add_u64 v[22:23], v[18:19], 0, s[36:37]
	global_load_dwordx4 v[24:27], v[22:23], off
	global_load_dwordx4 v[28:31], v[22:23], off offset:256
	v_mov_b32_e32 v2, 0
	v_mov_b32_e32 v3, 0
	v_mov_b32_e32 v4, 0
	v_mov_b32_e32 v5, 0
	v_mov_b32_e32 v6, 0
	v_mov_b32_e32 v7, 0
	v_mov_b32_e32 v8, 0
	v_mov_b32_e32 v9, 0
	s_and_b64 vcc, exec, s[0:1]
	s_cbranch_vccnz .Lmg_m6
	v_lshrrev_b32_e32 v2, 1, v222
	v_add_u32_e32 v2, 0x12060, v2
	ds_read_b64 v[2:3], v2
	v_mov_b32_e32 v4, v223
	v_mov_b32_e32 v5, v250
	s_mov_b32 s36, 0x50000
	v_lshl_add_u64 v[22:23], v[20:21], 0, s[36:37]
	global_load_dwordx2 v[6:7], v[22:23], off offset:256 sc1
	global_load_dwordx2 v[8:9], v[22:23], off offset:264 sc1
	s_waitcnt lgkmcnt(0)
.Lmg_m6:
	s_waitcnt vmcnt(4)
	v_lshlrev_b32_e32 v172, 16, v164
	v_and_b32_e32 v173, 0xffff0000, v164
	v_lshlrev_b32_e32 v174, 16, v10
	v_and_b32_e32 v175, 0xffff0000, v10
	v_pk_fma_f32 v[78:79], v[78:79], v[172:173], v[174:175]
	v_lshlrev_b32_e32 v176, 16, v165
	v_and_b32_e32 v177, 0xffff0000, v165
	v_lshlrev_b32_e32 v180, 16, v11
	v_and_b32_e32 v181, 0xffff0000, v11
	v_pk_fma_f32 v[80:81], v[80:81], v[176:177], v[180:181]
	v_lshlrev_b32_e32 v172, 16, v166
	v_and_b32_e32 v173, 0xffff0000, v166
	v_lshlrev_b32_e32 v174, 16, v12
	v_and_b32_e32 v175, 0xffff0000, v12
	v_pk_fma_f32 v[74:75], v[74:75], v[172:173], v[174:175]
	v_lshlrev_b32_e32 v176, 16, v167
	v_and_b32_e32 v177, 0xffff0000, v167
	v_lshlrev_b32_e32 v180, 16, v13
	v_and_b32_e32 v181, 0xffff0000, v13
	v_pk_fma_f32 v[76:77], v[76:77], v[176:177], v[180:181]
	v_cvt_pk_bf16_f32 v194, v78, v79
	v_cvt_pk_bf16_f32 v195, v80, v81
	v_cvt_pk_bf16_f32 v196, v74, v75
	v_cvt_pk_bf16_f32 v197, v76, v77
	s_mov_b32 s36, 0x48000
	v_lshl_add_u64 v[22:23], v[20:21], 0, s[36:37]
	ds_write_b128 v222, v[194:197] offset:16192
	s_mov_b64 exec, s[34:35]
	global_store_dwordx4 v[22:23], v[194:197], off
	s_mov_b64 exec, -1
	s_nop 1
	v_lshlrev_b32_e32 v172, 16, v168
	v_and_b32_e32 v173, 0xffff0000, v168
	v_lshlrev_b32_e32 v174, 16, v14
	v_and_b32_e32 v175, 0xffff0000, v14
	v_pk_fma_f32 v[70:71], v[70:71], v[172:173], v[174:175]
	v_lshlrev_b32_e32 v176, 16, v169
	v_and_b32_e32 v177, 0xffff0000, v169
	v_lshlrev_b32_e32 v180, 16, v15
	v_and_b32_e32 v181, 0xffff0000, v15
	v_pk_fma_f32 v[72:73], v[72:73], v[176:177], v[180:181]
	v_lshlrev_b32_e32 v172, 16, v170
	v_and_b32_e32 v173, 0xffff0000, v170
	v_lshlrev_b32_e32 v174, 16, v16
	v_and_b32_e32 v175, 0xffff0000, v16
	v_pk_fma_f32 v[66:67], v[66:67], v[172:173], v[174:175]
	v_lshlrev_b32_e32 v176, 16, v171
	v_and_b32_e32 v177, 0xffff0000, v171
	v_lshlrev_b32_e32 v180, 16, v17
	v_and_b32_e32 v181, 0xffff0000, v17
	v_pk_fma_f32 v[68:69], v[68:69], v[176:177], v[180:181]
	v_cvt_pk_bf16_f32 v194, v70, v71
	v_cvt_pk_bf16_f32 v195, v72, v73
	v_cvt_pk_bf16_f32 v196, v66, v67
	v_cvt_pk_bf16_f32 v197, v68, v69
	ds_write_b128 v222, v[194:197] offset:24384
	s_mov_b64 exec, s[34:35]
	global_store_dwordx4 v[22:23], v[194:197], off offset:256
	s_mov_b64 exec, -1
	s_nop 1
	s_mov_b32 s36, 0x108000
	v_lshl_add_u64 v[22:23], v[18:19], 0, s[36:37]
	global_load_dwordx4 v[164:167], v[22:23], off
	global_load_dwordx4 v[168:171], v[22:23], off offset:256
	v_mov_b32_e32 v10, 0
	v_mov_b32_e32 v11, 0
	v_mov_b32_e32 v12, 0
	v_mov_b32_e32 v13, 0
	v_mov_b32_e32 v14, 0
	v_mov_b32_e32 v15, 0
	v_mov_b32_e32 v16, 0
	v_mov_b32_e32 v17, 0
	s_and_b64 vcc, exec, s[0:1]
	s_cbranch_vccnz .Lmg_m7
	s_mov_b32 s36, 0x58000
	v_lshl_add_u64 v[22:23], v[20:21], 0, s[36:37]
	global_load_dwordx2 v[10:11], v[22:23], off sc1
	global_load_dwordx2 v[12:13], v[22:23], off offset:8 sc1
	global_load_dwordx2 v[14:15], v[22:23], off offset:256 sc1
	global_load_dwordx2 v[16:17], v[22:23], off offset:264 sc1
.Lmg_m7:
	s_waitcnt vmcnt(4)
	v_lshlrev_b32_e32 v172, 16, v24
	v_and_b32_e32 v173, 0xffff0000, v24
	v_lshlrev_b32_e32 v174, 16, v2
	v_and_b32_e32 v175, 0xffff0000, v2
	v_pk_fma_f32 v[62:63], v[62:63], v[172:173], v[174:175]
	v_lshlrev_b32_e32 v176, 16, v25
	v_and_b32_e32 v177, 0xffff0000, v25
	v_lshlrev_b32_e32 v180, 16, v3
	v_and_b32_e32 v181, 0xffff0000, v3
	v_pk_fma_f32 v[64:65], v[64:65], v[176:177], v[180:181]
	v_lshlrev_b32_e32 v172, 16, v26
	v_and_b32_e32 v173, 0xffff0000, v26
	v_lshlrev_b32_e32 v174, 16, v4
	v_and_b32_e32 v175, 0xffff0000, v4
	v_pk_fma_f32 v[58:59], v[58:59], v[172:173], v[174:175]
	v_lshlrev_b32_e32 v176, 16, v27
	v_and_b32_e32 v177, 0xffff0000, v27
	v_lshlrev_b32_e32 v180, 16, v5
	v_and_b32_e32 v181, 0xffff0000, v5
	v_pk_fma_f32 v[60:61], v[60:61], v[176:177], v[180:181]
	v_cvt_pk_bf16_f32 v194, v62, v63
	v_cvt_pk_bf16_f32 v195, v64, v65
	v_cvt_pk_bf16_f32 v196, v58, v59
	v_cvt_pk_bf16_f32 v197, v60, v61
	s_mov_b32 s36, 0x50000
	v_lshl_add_u64 v[22:23], v[20:21], 0, s[36:37]
	v_mov_b32_e32 v223, v196
	v_mov_b32_e32 v250, v197
	v_lshrrev_b32_e32 v172, 1, v222
	v_add_u32_e32 v172, 0x12060, v172
	ds_write_b64 v172, v[194:195]
	s_mov_b64 exec, s[34:35]
	global_store_dwordx4 v[22:23], v[194:197], off
	s_mov_b64 exec, -1
	s_nop 1
	v_lshlrev_b32_e32 v172, 16, v28
	v_and_b32_e32 v173, 0xffff0000, v28
	v_lshlrev_b32_e32 v174, 16, v6
	v_and_b32_e32 v175, 0xffff0000, v6
	v_pk_fma_f32 v[54:55], v[54:55], v[172:173], v[174:175]
	v_lshlrev_b32_e32 v176, 16, v29
	v_and_b32_e32 v177, 0xffff0000, v29
	v_lshlrev_b32_e32 v180, 16, v7
	v_and_b32_e32 v181, 0xffff0000, v7
	v_pk_fma_f32 v[56:57], v[56:57], v[176:177], v[180:181]
	v_lshlrev_b32_e32 v172, 16, v30
	v_and_b32_e32 v173, 0xffff0000, v30
	v_lshlrev_b32_e32 v174, 16, v8
	v_and_b32_e32 v175, 0xffff0000, v8
	v_pk_fma_f32 v[50:51], v[50:51], v[172:173], v[174:175]
	v_lshlrev_b32_e32 v176, 16, v31
	v_and_b32_e32 v177, 0xffff0000, v31
	v_lshlrev_b32_e32 v180, 16, v9
	v_and_b32_e32 v181, 0xffff0000, v9
	v_pk_fma_f32 v[52:53], v[52:53], v[176:177], v[180:181]
	v_cvt_pk_bf16_f32 v194, v54, v55
	v_cvt_pk_bf16_f32 v195, v56, v57
	v_cvt_pk_bf16_f32 v196, v50, v51
	v_cvt_pk_bf16_f32 v197, v52, v53
	global_store_dwordx4 v[22:23], v[194:197], off offset:256
	s_nop 1
	s_waitcnt vmcnt(2)
	v_lshlrev_b32_e32 v172, 16, v164
	v_and_b32_e32 v173, 0xffff0000, v164
	v_lshlrev_b32_e32 v174, 16, v10
	v_and_b32_e32 v175, 0xffff0000, v10
	v_pk_fma_f32 v[46:47], v[46:47], v[172:173], v[174:175]
	v_lshlrev_b32_e32 v176, 16, v165
	v_and_b32_e32 v177, 0xffff0000, v165
	v_lshlrev_b32_e32 v180, 16, v11
	v_and_b32_e32 v181, 0xffff0000, v11
	v_pk_fma_f32 v[48:49], v[48:49], v[176:177], v[180:181]
	v_lshlrev_b32_e32 v172, 16, v166
	v_and_b32_e32 v173, 0xffff0000, v166
	v_lshlrev_b32_e32 v174, 16, v12
	v_and_b32_e32 v175, 0xffff0000, v12
	v_pk_fma_f32 v[42:43], v[42:43], v[172:173], v[174:175]
	v_lshlrev_b32_e32 v176, 16, v167
	v_and_b32_e32 v177, 0xffff0000, v167
	v_lshlrev_b32_e32 v180, 16, v13
	v_and_b32_e32 v181, 0xffff0000, v13
	v_pk_fma_f32 v[44:45], v[44:45], v[176:177], v[180:181]
	v_cvt_pk_bf16_f32 v194, v46, v47
	v_cvt_pk_bf16_f32 v195, v48, v49
	v_cvt_pk_bf16_f32 v196, v42, v43
	v_cvt_pk_bf16_f32 v197, v44, v45
	s_mov_b32 s36, 0x58000
	v_lshl_add_u64 v[22:23], v[20:21], 0, s[36:37]
	global_store_dwordx4 v[22:23], v[194:197], off
	s_nop 1
	v_lshlrev_b32_e32 v172, 16, v168
	v_and_b32_e32 v173, 0xffff0000, v168
	v_lshlrev_b32_e32 v174, 16, v14
	v_and_b32_e32 v175, 0xffff0000, v14
	v_pk_fma_f32 v[38:39], v[38:39], v[172:173], v[174:175]
	v_lshlrev_b32_e32 v176, 16, v169
	v_and_b32_e32 v177, 0xffff0000, v169
	v_lshlrev_b32_e32 v180, 16, v15
	v_and_b32_e32 v181, 0xffff0000, v15
	v_pk_fma_f32 v[40:41], v[40:41], v[176:177], v[180:181]
	v_lshlrev_b32_e32 v172, 16, v170
	v_and_b32_e32 v173, 0xffff0000, v170
	v_lshlrev_b32_e32 v174, 16, v16
	v_and_b32_e32 v175, 0xffff0000, v16
	v_pk_fma_f32 v[34:35], v[34:35], v[172:173], v[174:175]
	v_lshlrev_b32_e32 v176, 16, v171
	v_and_b32_e32 v177, 0xffff0000, v171
	v_lshlrev_b32_e32 v180, 16, v17
	v_and_b32_e32 v181, 0xffff0000, v17
	v_pk_fma_f32 v[36:37], v[36:37], v[176:177], v[180:181]
	v_cvt_pk_bf16_f32 v194, v38, v39
	v_cvt_pk_bf16_f32 v195, v40, v41
	v_cvt_pk_bf16_f32 v196, v34, v35
	v_cvt_pk_bf16_f32 v197, v36, v37
	global_store_dwordx4 v[22:23], v[194:197], off offset:256
	s_nop 1
	s_andn2_b64 vcc, exec, s[38:39]
	s_mov_b64 s[0:1], -1
	s_cbranch_vccnz .LBB0_795
	v_readlane_b32 s28, v253, 4
	v_readlane_b32 s30, v253, 6
	v_readlane_b32 s31, v253, 7
	v_readlane_b32 s29, v253, 5
	s_and_b64 vcc, exec, s[8:9]
	v_mov_b64_e32 v[36:37], s[30:31]
	v_mov_b64_e32 v[160:161], s[30:31]
	v_mov_b64_e32 v[156:157], s[30:31]
	v_mov_b64_e32 v[144:145], s[30:31]
	v_mov_b64_e32 v[140:141], s[30:31]
	v_mov_b64_e32 v[128:129], s[30:31]
	v_mov_b64_e32 v[124:125], s[30:31]
	v_mov_b64_e32 v[112:113], s[30:31]
	v_mov_b64_e32 v[108:109], s[30:31]
	v_mov_b64_e32 v[152:153], s[30:31]
	v_mov_b64_e32 v[148:149], s[30:31]
	v_mov_b64_e32 v[136:137], s[30:31]
	v_mov_b64_e32 v[132:133], s[30:31]
	v_mov_b64_e32 v[120:121], s[30:31]
	v_mov_b64_e32 v[116:117], s[30:31]
	v_mov_b64_e32 v[104:105], s[30:31]
	v_mov_b64_e32 v[100:101], s[30:31]
	v_mov_b64_e32 v[96:97], s[30:31]
	v_mov_b64_e32 v[92:93], s[30:31]
	v_mov_b64_e32 v[80:81], s[30:31]
	v_mov_b64_e32 v[76:77], s[30:31]
	v_mov_b64_e32 v[64:65], s[30:31]
	v_mov_b64_e32 v[60:61], s[30:31]
	v_mov_b64_e32 v[48:49], s[30:31]
	v_mov_b64_e32 v[44:45], s[30:31]
	v_mov_b64_e32 v[88:89], s[30:31]
	v_mov_b64_e32 v[84:85], s[30:31]
	v_mov_b64_e32 v[72:73], s[30:31]
	v_mov_b64_e32 v[68:69], s[30:31]
	v_mov_b64_e32 v[56:57], s[30:31]
	v_mov_b64_e32 v[52:53], s[30:31]
	v_mov_b64_e32 v[40:41], s[30:31]
	v_mov_b64_e32 v[34:35], s[28:29]
	v_mov_b64_e32 v[158:159], s[28:29]
	v_mov_b64_e32 v[154:155], s[28:29]
	v_mov_b64_e32 v[142:143], s[28:29]
	v_mov_b64_e32 v[138:139], s[28:29]
	v_mov_b64_e32 v[126:127], s[28:29]
	v_mov_b64_e32 v[122:123], s[28:29]
	v_mov_b64_e32 v[110:111], s[28:29]
	v_mov_b64_e32 v[106:107], s[28:29]
	v_mov_b64_e32 v[150:151], s[28:29]
	v_mov_b64_e32 v[146:147], s[28:29]
	v_mov_b64_e32 v[134:135], s[28:29]
	v_mov_b64_e32 v[130:131], s[28:29]
	v_mov_b64_e32 v[118:119], s[28:29]
	v_mov_b64_e32 v[114:115], s[28:29]
	v_mov_b64_e32 v[102:103], s[28:29]
	v_mov_b64_e32 v[98:99], s[28:29]
	v_mov_b64_e32 v[94:95], s[28:29]
	v_mov_b64_e32 v[90:91], s[28:29]
	v_mov_b64_e32 v[78:79], s[28:29]
	v_mov_b64_e32 v[74:75], s[28:29]
	v_mov_b64_e32 v[62:63], s[28:29]
	v_mov_b64_e32 v[58:59], s[28:29]
	v_mov_b64_e32 v[46:47], s[28:29]
	v_mov_b64_e32 v[42:43], s[28:29]
	v_mov_b64_e32 v[86:87], s[28:29]
	v_mov_b64_e32 v[82:83], s[28:29]
	v_mov_b64_e32 v[70:71], s[28:29]
	v_mov_b64_e32 v[66:67], s[28:29]
	v_mov_b64_e32 v[54:55], s[28:29]
	v_mov_b64_e32 v[50:51], s[28:29]
	v_mov_b64_e32 v[38:39], s[28:29]
	s_cbranch_vccz .LBB0_794
	s_barrier
	s_branch .LBB0_794
